# combination: tail-round weight conversion incl. layer-1 MoE down-projection tail and layer-0 w_out/ffn13 deferral, DPP wave reductions, N1 next-row cache warming
# speedup vs baseline: 1.0080x; 1.0080x over previous
.LBB0_390:
	s_waitcnt vmcnt(7)
	v_pk_mul_f32 v[96:97], v[64:65], v[64:65]
	v_pk_mul_f32 v[98:99], v[62:63], v[62:63]
	s_waitcnt vmcnt(6)
	v_pk_mul_f32 v[92:93], v[60:61], v[60:61]
	v_pk_mul_f32 v[94:95], v[58:59], v[58:59]
	v_pk_mov_b32 v[100:101], v[98:99], v[96:97] op_sel:[1,0]
	v_mov_b32_e32 v99, v97
	v_pk_add_f32 v[96:97], v[100:101], v[98:99]
	v_pk_mov_b32 v[98:99], v[94:95], v[92:93] op_sel:[1,0]
	v_mov_b32_e32 v95, v93
	v_pk_add_f32 v[92:93], v[98:99], v[94:95]
	v_pk_add_f32 v[96:97], v[96:97], v[96:97] op_sel_hi:[0,1]
	v_pk_add_f32 v[92:93], v[92:93], v[92:93] op_sel_hi:[0,1]
	s_waitcnt vmcnt(5)
	v_mul_f32_e32 v92, v54, v54
	v_pk_fma_f32 v[94:95], v[54:55], v[54:55], v[92:93] op_sel_hi:[1,1,0]
	v_mul_f32_e32 v92, v56, v56
	v_pk_fma_f32 v[98:99], v[56:57], v[56:57], v[92:93] op_sel_hi:[1,1,0]
	s_waitcnt vmcnt(4)
	v_mul_f32_e32 v94, v50, v50
	v_mul_f32_e32 v98, v51, v51
	v_mul_f32_e32 v96, v52, v52
	v_mul_f32_e32 v92, v53, v53
	v_pk_add_f32 v[94:95], v[94:95], v[98:99]
	v_pk_add_f32 v[92:93], v[96:97], v[92:93]
	s_mov_b32 s0, 0xf800000
	v_pk_add_f32 v[92:93], v[94:95], v[92:93]
	s_mov_b32 s3, 0x42fe0000
	v_add_f32_e32 v91, v92, v93
	s_waitcnt lgkmcnt(0)
	s_nop 1
	v_add_f32_dpp v91, v91, v91 quad_perm:[1,0,3,2] row_mask:0xf bank_mask:0xf
	v_readlane_b32 s40, v251, 5
	v_readlane_b32 s46, v251, 11
	v_readlane_b32 s47, v251, 12
	v_readlane_b32 s41, v251, 6
	s_nop 1
	v_add_f32_dpp v91, v91, v91 quad_perm:[2,3,0,1] row_mask:0xf bank_mask:0xf
	v_readlane_b32 s42, v251, 7
	v_readlane_b32 s43, v251, 8
	v_readlane_b32 s44, v251, 9
	v_readlane_b32 s45, v251, 10
	s_nop 1
	v_add_f32_dpp v91, v91, v91 row_half_mirror row_mask:0xf bank_mask:0xf
	s_nop 1
	v_add_f32_dpp v91, v91, v91 row_mirror row_mask:0xf bank_mask:0xf
	s_nop 1
	v_readlane_b32 s98, v91, 0
	v_readlane_b32 s99, v91, 16
	v_readlane_b32 s100, v91, 32
	v_readlane_b32 s101, v91, 48
	s_nop 1
	v_mov_b32_e32 v92, s99
	v_add_f32_e32 v92, s98, v92
	v_mov_b32_e32 v91, s101
	v_add_f32_e32 v91, s100, v91
	v_add_f32_e32 v91, v92, v91
	v_fmamk_f32 v91, v91, 0x3a800000, v241
	v_mul_f32_e32 v92, 0x4f800000, v91
	v_cmp_gt_f32_e32 vcc, s0, v91
	s_nop 1
	v_cndmask_b32_e32 v91, v91, v92, vcc
	v_sqrt_f32_e32 v94, v91
	v_pk_add_f32 v[92:93], v[28:29], 1.0 op_sel_hi:[1,0]
	v_add_u32_e32 v95, -1, v94
	v_add_u32_e32 v96, 1, v94
	v_fma_f32 v97, -v95, v94, v91
	v_fma_f32 v98, -v96, v94, v91
	v_cmp_ge_f32_e64 s[0:1], 0, v97
	s_nop 1
	v_cndmask_b32_e64 v94, v94, v95, s[0:1]
	v_cmp_lt_f32_e64 s[0:1], 0, v98
	s_nop 1
	v_cndmask_b32_e64 v94, v94, v96, s[0:1]
	v_mul_f32_e32 v95, 0x37800000, v94
	v_cndmask_b32_e32 v94, v94, v95, vcc
	v_cmp_class_f32_e32 vcc, v91, v188
	s_nop 1
	v_cndmask_b32_e32 v91, v94, v91, vcc
	v_div_scale_f32 v96, s[0:1], v91, v91, 1.0
	v_rcp_f32_e32 v97, v96
	v_div_scale_f32 v98, vcc, 1.0, v91, 1.0
	v_pk_add_f32 v[94:95], v[26:27], 1.0 op_sel_hi:[1,0]
	v_fma_f32 v99, -v96, v97, 1.0
	v_fmac_f32_e32 v97, v99, v97
	v_mul_f32_e32 v99, v98, v97
	v_fma_f32 v100, -v96, v99, v98
	v_fmac_f32_e32 v99, v100, v97
	v_fma_f32 v96, -v96, v99, v98
	v_div_fmas_f32 v96, v96, v97, v99
	v_div_fixup_f32 v96, v96, v91, 1.0
	v_pk_mul_f32 v[64:65], v[64:65], v[96:97] op_sel_hi:[1,0]
	v_pk_mul_f32 v[62:63], v[62:63], v[96:97] op_sel_hi:[1,0]
	v_pk_mul_f32 v[64:65], v[16:17], v[64:65]
	v_pk_mul_f32 v[62:63], v[14:15], v[62:63]
	v_pk_mul_f32 v[60:61], v[60:61], v[96:97] op_sel_hi:[1,0]
	v_pk_mul_f32 v[58:59], v[58:59], v[96:97] op_sel_hi:[1,0]
	v_pk_fma_f32 v[64:65], v[92:93], v[64:65], v[20:21]
	v_pk_fma_f32 v[62:63], v[94:95], v[62:63], v[18:19]
	v_pk_mul_f32 v[58:59], v[10:11], v[58:59]
	v_pk_mul_f32 v[60:61], v[12:13], v[60:61]
	v_pk_add_f32 v[92:93], v[24:25], 1.0 op_sel_hi:[1,0]
	v_pk_add_f32 v[94:95], v[22:23], 1.0 op_sel_hi:[1,0]
	v_pk_mul_f32 v[56:57], v[56:57], v[96:97] op_sel_hi:[1,0]
	v_pk_mul_f32 v[54:55], v[54:55], v[96:97] op_sel_hi:[1,0]
	v_pk_fma_f32 v[60:61], v[92:93], v[60:61], v[32:33]
	v_pk_fma_f32 v[58:59], v[94:95], v[58:59], v[30:31]
	v_pk_mul_f32 v[54:55], v[6:7], v[54:55]
	v_pk_mul_f32 v[56:57], v[8:9], v[56:57]
	v_pk_add_f32 v[92:93], v[40:41], 1.0 op_sel_hi:[1,0]
	v_pk_add_f32 v[94:95], v[38:39], 1.0 op_sel_hi:[1,0]
	v_pk_mul_f32 v[52:53], v[52:53], v[96:97] op_sel_hi:[1,0]
	v_pk_mul_f32 v[50:51], v[50:51], v[96:97] op_sel_hi:[1,0]
	v_pk_fma_f32 v[56:57], v[92:93], v[56:57], v[44:45]
	v_pk_fma_f32 v[54:55], v[94:95], v[54:55], v[42:43]
	v_pk_mul_f32 v[50:51], v[2:3], v[50:51]
	v_pk_mul_f32 v[52:53], v[4:5], v[52:53]
	v_pk_add_f32 v[92:93], v[36:37], 1.0 op_sel_hi:[1,0]
	v_pk_add_f32 v[94:95], v[34:35], 1.0 op_sel_hi:[1,0]
	v_pk_fma_f32 v[52:53], v[92:93], v[52:53], v[48:49]
	v_pk_fma_f32 v[92:93], v[94:95], v[50:51], v[46:47]
	v_max_f32_e64 v50, |v62|, |v63|
	v_max_f32_e64 v51, |v64|, |v65|
	v_max3_f32 v50, v50, 0, v51
	v_max_f32_e64 v51, |v58|, |v59|
	v_max_f32_e64 v91, |v60|, |v61|
	v_max3_f32 v50, v50, v51, v91
	v_max_f32_e64 v51, |v54|, |v55|
	v_max_f32_e64 v91, |v56|, |v57|
	v_max3_f32 v50, v50, v51, v91
	v_max_f32_e64 v51, |v92|, |v93|
	v_max_f32_e64 v91, |v52|, |v53|
	v_max3_f32 v50, v50, v51, v91
	s_waitcnt lgkmcnt(0)
	s_nop 1
	v_max_f32_dpp v50, v50, v50 quad_perm:[1,0,3,2] row_mask:0xf bank_mask:0xf
	s_nop 1
	v_max_f32_dpp v50, v50, v50 quad_perm:[2,3,0,1] row_mask:0xf bank_mask:0xf
	s_nop 1
	v_max_f32_dpp v50, v50, v50 row_half_mirror row_mask:0xf bank_mask:0xf
	s_nop 1
	v_max_f32_dpp v50, v50, v50 row_mirror row_mask:0xf bank_mask:0xf
	s_nop 1
	v_readlane_b32 s98, v50, 0
	v_readlane_b32 s99, v50, 16
	v_readlane_b32 s100, v50, 32
	v_readlane_b32 s101, v50, 48
	s_nop 1
	v_mov_b32_e32 v51, s99
	v_max_f32_e32 v51, s98, v51
	v_mov_b32_e32 v50, s101
	v_max_f32_e32 v50, s100, v50
	v_max_f32_e32 v50, v51, v50
	v_div_scale_f32 v51, s[0:1], v50, v50, s3
	v_rcp_f32_e32 v91, v51
	s_mov_b32 s0, 0x40c0c00
	s_mov_b32 s1, 0x8900000
	v_fma_f32 v94, -v51, v91, 1.0
	v_fmac_f32_e32 v91, v94, v91
	v_div_scale_f32 v94, vcc, s3, v50, s3
	v_mul_f32_e32 v95, v94, v91
	v_fma_f32 v96, -v51, v95, v94
	v_fmac_f32_e32 v95, v96, v91
	v_fma_f32 v51, -v51, v95, v94
	v_div_fmas_f32 v51, v51, v91, v95
	v_div_fixup_f32 v51, v51, v50, s3
	v_cmp_lt_f32_e32 vcc, 0, v50
	v_lshl_add_u64 v[94:95], s[46:47], 0, v[82:83]
	s_nop 0
	v_cndmask_b32_e32 v51, 0, v51, vcc
	v_mul_f32_e32 v63, v63, v51
	v_mul_f32_e32 v62, v62, v51
	v_rndne_f32_e32 v63, v63
	v_mul_f32_e32 v64, v64, v51
	v_mul_f32_e32 v65, v65, v51
	v_mul_f32_e32 v55, v55, v51
	v_rndne_f32_e32 v62, v62
	v_cvt_i32_f32_e32 v63, v63
	v_rndne_f32_e32 v64, v64
	v_rndne_f32_e32 v65, v65
	v_mul_f32_e32 v54, v54, v51
	v_rndne_f32_e32 v55, v55
	v_mul_f32_e32 v56, v56, v51
	v_mul_f32_e32 v57, v57, v51
	v_cvt_i32_f32_e32 v62, v62
	v_cvt_i32_f32_sdwa v64, v64 dst_sel:WORD_1 dst_unused:UNUSED_PAD src0_sel:DWORD
	v_cvt_i32_f32_e32 v65, v65
	v_rndne_f32_e32 v54, v54
	v_cvt_i32_f32_e32 v55, v55
	v_rndne_f32_e32 v56, v56
	v_rndne_f32_e32 v57, v57
	v_cvt_i32_f32_e32 v54, v54
	v_cvt_i32_f32_sdwa v56, v56 dst_sel:WORD_1 dst_unused:UNUSED_PAD src0_sel:DWORD
	v_cvt_i32_f32_e32 v57, v57
	v_lshlrev_b32_e32 v63, 8, v63
	v_and_b32_e32 v63, 0xff00, v63
	v_and_b32_e32 v64, 0xff0000, v64
	v_perm_b32 v62, v65, v62, s0
	v_lshlrev_b32_e32 v55, 8, v55
	v_or3_b32 v64, v62, v63, v64
	v_add_co_u32_e32 v62, vcc, s1, v94
	v_and_b32_e32 v55, 0xff00, v55
	v_and_b32_e32 v56, 0xff0000, v56
	v_perm_b32 v54, v57, v54, s0
	v_addc_co_u32_e32 v63, vcc, 0, v95, vcc
	v_mul_f32_e32 v59, v59, v51
	v_or3_b32 v54, v54, v55, v56
	v_mul_f32_e32 v55, v93, v51
	v_mul_f32_e32 v58, v58, v51
	v_rndne_f32_e32 v59, v59
	v_mul_f32_e32 v60, v60, v51
	v_mul_f32_e32 v61, v61, v51
	global_store_dword v[62:63], v54, off offset:512
	v_mul_f32_e32 v54, v92, v51
	v_rndne_f32_e32 v55, v55
	v_mul_f32_e32 v52, v52, v51
	v_mul_f32_e32 v51, v53, v51
	v_rndne_f32_e32 v58, v58
	v_cvt_i32_f32_e32 v59, v59
	v_rndne_f32_e32 v60, v60
	v_rndne_f32_e32 v61, v61
	v_rndne_f32_e32 v54, v54
	v_cvt_i32_f32_e32 v55, v55
	v_rndne_f32_e32 v52, v52
	v_rndne_f32_e32 v51, v51
	v_cvt_i32_f32_e32 v58, v58
	v_cvt_i32_f32_sdwa v60, v60 dst_sel:WORD_1 dst_unused:UNUSED_PAD src0_sel:DWORD
	v_cvt_i32_f32_e32 v61, v61
	v_cvt_i32_f32_e32 v54, v54
	v_cvt_i32_f32_sdwa v52, v52 dst_sel:WORD_1 dst_unused:UNUSED_PAD src0_sel:DWORD
	v_cvt_i32_f32_e32 v51, v51
	v_lshlrev_b32_e32 v59, 8, v59
	v_lshlrev_b32_e32 v53, 8, v55
	v_and_b32_e32 v59, 0xff00, v59
	v_and_b32_e32 v60, 0xff0000, v60
	v_perm_b32 v58, v61, v58, s0
	v_and_b32_e32 v53, 0xff00, v53
	v_and_b32_e32 v52, 0xff0000, v52
	v_perm_b32 v51, v51, v54, s0
	v_or3_b32 v58, v58, v59, v60
	v_or3_b32 v51, v51, v53, v52
	global_store_dword v[62:63], v64, off
	global_store_dword v[62:63], v58, off offset:256
	global_store_dword v[62:63], v51, off offset:768
	s_and_saveexec_b64 s[0:1], s[36:37]
	s_cbranch_execz .LBB0_383
	v_readlane_b32 s40, v251, 5
	v_readlane_b32 s46, v251, 11
	v_readlane_b32 s47, v251, 12
	v_mul_f32_e32 v52, 0x3c010204, v50
	v_readlane_b32 s41, v251, 6
	v_lshl_add_u64 v[50:51], s[46:47], 0, v[78:79]
	v_readlane_b32 s42, v251, 7
	v_readlane_b32 s43, v251, 8
	v_readlane_b32 s44, v251, 9
	v_readlane_b32 s45, v251, 10
	global_store_dword v[50:51], v52, off
	s_branch .LBB0_383
